# baseline (speedup 1.0000x reference)
_Z16sum_layer_kernelPKfS0_Pf:
	s_load_dwordx4 s[4:7], s[0:1], 0x0
	s_load_dwordx2 s[8:9], s[0:1], 0x10
	v_lshrrev_b32_e32 v42, 6, v0
	v_bfe_u32 v41, v0, 5, 1
	v_and_b32_e32 v40, 31, v0
	v_readfirstlane_b32 s23, v42
	v_and_b32_e32 v43, 7, v0
	v_bfe_u32 v44, v0, 3, 3
	s_lshl_b32 s3, s2, 12
	s_lshl_b32 s19, s2, 7
	s_lshl_b32 s23, s23, 12
	v_lshlrev_b32_e32 v1, 11, v41
	v_lshl_or_b32 v1, v40, 2, v1
	s_mov_b32 m0, s23
	v_lshrrev_b32_e32 v46, 1, v44
	v_xor_b32_e32 v46, v43, v46
	v_lshlrev_b32_e32 v46, 4, v46
	v_lshl_add_u32 v35, v44, 16, v46
	v_lshl_add_u32 v35, v42, 21, v35
	v_add_u32_e32 v35, s19, v35
	v_xor_b32_e32 v86, 64, v35
	s_mov_b32 s20, 0x7fc00
	s_mov_b32 s21, 0xff800
	s_mov_b32 s22, 0x17f400
	s_mov_b32 s14, 0x200000
	s_mov_b32 s15, 0x20000
	v_and_b32_e32 v45, 63, v0
	v_lshlrev_b32_e32 v37, 4, v45
	s_add_u32 s54, s23, 0x4000
	s_waitcnt lgkmcnt(0)
	s_mov_b32 s12, s6
	s_and_b32 s13, s7, 0xffff
	s_and_b32 s5, s5, 0xffff
	s_mov_b32 s6, 0x800000
	s_mov_b32 s7, s15
	s_mov_b32 m0, s54
	s_nop 0
	buffer_load_dwordx4 v37, s[12:15], s3 offen sc0 nt lds
	buffer_load_dwordx4 v37, s[12:15], s3 offen offset:1024 sc0 nt lds
	buffer_load_dwordx4 v37, s[12:15], s3 offen offset:2048 sc0 nt lds
	buffer_load_dwordx4 v37, s[12:15], s3 offen offset:3072 sc0 nt lds
	s_mov_b32 m0, s23
	s_nop 0
	buffer_load_dwordx4 v35, s[4:7], 0 offen nt lds
	buffer_load_dwordx4 v86, s[4:7], s20 offen offset:1024 nt lds
	buffer_load_dwordx4 v35, s[4:7], s21 offen offset:2048 nt lds
	buffer_load_dwordx4 v86, s[4:7], s22 offen offset:3072 nt lds
	v_and_b32_e32 v45, 63, v0
	v_lshlrev_b32_e32 v36, 2, v40
	v_lshl_add_u32 v36, v41, 18, v36
	v_lshl_add_u32 v36, v42, 21, v36
	v_add_u32_e32 v36, s19, v36
	v_bfe_u32 v47, v40, 1, 3
	v_lshlrev_b32_e32 v39, 2, v41
	v_xor_b32_e32 v39, v39, v47
	v_lshlrev_b32_e32 v39, 4, v39
	v_lshl_add_u32 v39, v40, 7, v39
	v_lshl_add_u32 v39, v42, 12, v39
	v_xor_b32_e32 v81, 16, v39
	v_xor_b32_e32 v82, 32, v39
	v_xor_b32_e32 v83, 48, v39
	v_cmp_gt_u32_e32 vcc, 32, v45
	v_mov_b32_e32 v34, 0xc1600000
	v_mov_b32_e32 v84, 0x3fb8aa3b
	v_mov_b32_e32 v85, 0x3f317218
	s_lshl_b32 s24, 1, 16
	s_lshl_b32 s25, 2, 16
	s_lshl_b32 s26, 3, 16
	s_lshl_b32 s27, 8, 16
	s_lshl_b32 s28, 9, 16
	s_lshl_b32 s29, 10, 16
	s_lshl_b32 s30, 11, 16
	s_lshl_b32 s31, 16, 16
	s_lshl_b32 s32, 17, 16
	s_lshl_b32 s33, 18, 16
	s_lshl_b32 s34, 19, 16
	s_lshl_b32 s35, 24, 16
	s_lshl_b32 s36, 25, 16
	s_lshl_b32 s37, 26, 16
	s_lshl_b32 s38, 27, 16
	s_and_b32 s9, s9, 0xffff
	s_mov_b32 s10, s6
	s_mov_b32 s11, s15
	v_lshl_add_u32 v38, v42, 12, v1
	v_add_u32_e32 v38, 0x4000, v38
	v_add_u32_e32 v87, 0x400, v38
	s_waitcnt vmcnt(4)
	ds_read2_b32 v[18:19], v38 offset0:0 offset1:32
	ds_read2_b32 v[20:21], v38 offset0:64 offset1:96
	ds_read2_b32 v[22:23], v38 offset0:128 offset1:160
	ds_read2_b32 v[24:25], v38 offset0:192 offset1:224
	ds_read2_b32 v[26:27], v87 offset0:0 offset1:32
	ds_read2_b32 v[28:29], v87 offset0:64 offset1:96
	ds_read2_b32 v[30:31], v87 offset0:128 offset1:160
	ds_read2_b32 v[32:33], v87 offset0:192 offset1:224
	s_waitcnt lgkmcnt(0)
	v_max3_f32 v48, v18, v19, v20
	v_max3_f32 v50, v21, v22, v23
	v_max3_f32 v48, v48, v24, v25
	v_max3_f32 v50, v50, v26, v27
	v_max3_f32 v48, v48, v28, v29
	v_max3_f32 v50, v50, v30, v31
	v_max3_f32 v48, v48, v32, v33
	v_max_f32_e32 v48, v48, v50
	v_mov_b32_e32 v50, v48
	s_nop 1
	v_permlane32_swap_b32_e32 v48, v50
	v_max_f32_e32 v48, v48, v50
	v_fmamk_f32 v48, v48, 0x3fb8aa3b, v34
	v_pk_fma_f32 v[18:19], v[18:19], v[84:85], v[48:49] op_sel_hi:[1,0,0] neg_lo:[0,0,1] neg_hi:[0,0,1]
	v_exp_f32_e32 v18, v18
	v_exp_f32_e32 v19, v19
	v_pk_fma_f32 v[20:21], v[20:21], v[84:85], v[48:49] op_sel_hi:[1,0,0] neg_lo:[0,0,1] neg_hi:[0,0,1]
	v_exp_f32_e32 v20, v20
	v_exp_f32_e32 v21, v21
	v_pk_fma_f32 v[22:23], v[22:23], v[84:85], v[48:49] op_sel_hi:[1,0,0] neg_lo:[0,0,1] neg_hi:[0,0,1]
	v_exp_f32_e32 v22, v22
	v_exp_f32_e32 v23, v23
	v_pk_fma_f32 v[24:25], v[24:25], v[84:85], v[48:49] op_sel_hi:[1,0,0] neg_lo:[0,0,1] neg_hi:[0,0,1]
	v_exp_f32_e32 v24, v24
	v_exp_f32_e32 v25, v25
	v_pk_fma_f32 v[26:27], v[26:27], v[84:85], v[48:49] op_sel_hi:[1,0,0] neg_lo:[0,0,1] neg_hi:[0,0,1]
	v_exp_f32_e32 v26, v26
	v_exp_f32_e32 v27, v27
	v_pk_fma_f32 v[28:29], v[28:29], v[84:85], v[48:49] op_sel_hi:[1,0,0] neg_lo:[0,0,1] neg_hi:[0,0,1]
	v_exp_f32_e32 v28, v28
	v_exp_f32_e32 v29, v29
	v_pk_fma_f32 v[30:31], v[30:31], v[84:85], v[48:49] op_sel_hi:[1,0,0] neg_lo:[0,0,1] neg_hi:[0,0,1]
	v_exp_f32_e32 v30, v30
	v_exp_f32_e32 v31, v31
	v_pk_fma_f32 v[32:33], v[32:33], v[84:85], v[48:49] op_sel_hi:[1,0,0] neg_lo:[0,0,1] neg_hi:[0,0,1]
	v_exp_f32_e32 v32, v32
	v_exp_f32_e32 v33, v33
	v_pk_add_f32 v[56:57], v[18:19], v[20:21]
	v_pk_add_f32 v[58:59], v[22:23], v[24:25]
	v_pk_add_f32 v[60:61], v[26:27], v[28:29]
	v_pk_add_f32 v[62:63], v[30:31], v[32:33]
	v_pk_add_f32 v[56:57], v[56:57], v[58:59]
	v_pk_add_f32 v[60:61], v[60:61], v[62:63]
	v_pk_add_f32 v[56:57], v[56:57], v[60:61]
	v_add_f32_e32 v50, v56, v57
	v_mov_b32_e32 v51, v50
	s_nop 1
	v_permlane32_swap_b32_e32 v50, v51
	v_add_f32_e32 v50, v50, v51
	v_log_f32_e32 v50, v50
	v_cvt_pk_f16_f32 v40, v18, v19
	v_cvt_pk_f16_f32 v41, v20, v21
	v_cvt_pk_f16_f32 v42, v22, v23
	v_cvt_pk_f16_f32 v43, v24, v25
	v_cvt_pk_f16_f32 v44, v26, v27
	v_cvt_pk_f16_f32 v45, v28, v29
	v_cvt_pk_f16_f32 v46, v30, v31
	v_cvt_pk_f16_f32 v47, v32, v33
	v_add_f32_e32 v50, 0x41600000, v50
	v_mul_f32_e32 v50, 0xbf317218, v50
	v_cndmask_b32_e64 v51, v50, 1.0, vcc
	s_waitcnt vmcnt(0)
	ds_read_b128 v[2:5], v39
	ds_read_b128 v[6:9], v81
	ds_read_b128 v[10:13], v82
	ds_read_b128 v[14:17], v83
	s_waitcnt lgkmcnt(2)
	v_max3_f32 v52, v2, v3, v4
	v_max3_f32 v53, v5, v6, v7
	v_max_f32_e32 v52, v52, v8
	v_max_f32_e32 v53, v53, v9
	s_waitcnt lgkmcnt(0)
	v_max3_f32 v52, v52, v10, v11
	v_max3_f32 v53, v53, v12, v13
	v_max3_f32 v52, v52, v14, v15
	v_max3_f32 v53, v53, v16, v17
	v_max_f32_e32 v52, v52, v53
	v_mov_b32_e32 v53, v52
	s_nop 1
	v_permlane32_swap_b32_e32 v52, v53
	v_max_f32_e32 v52, v52, v53
	v_cndmask_b32_e32 v54, 1.0, v52, vcc
	v_fmamk_f32 v48, v52, 0x3fb8aa3b, v34
	v_pk_fma_f32 v[2:3], v[2:3], v[84:85], v[48:49] op_sel_hi:[1,0,0] neg_lo:[0,0,1] neg_hi:[0,0,1]
	v_mfma_f32_32x32x2_f32 v[64:79], v54, v51, 0
	v_exp_f32_e32 v2, v2
	v_exp_f32_e32 v3, v3
	v_pk_fma_f32 v[4:5], v[4:5], v[84:85], v[48:49] op_sel_hi:[1,0,0] neg_lo:[0,0,1] neg_hi:[0,0,1]
	v_exp_f32_e32 v4, v4
	v_exp_f32_e32 v5, v5
	v_pk_fma_f32 v[6:7], v[6:7], v[84:85], v[48:49] op_sel_hi:[1,0,0] neg_lo:[0,0,1] neg_hi:[0,0,1]
	v_exp_f32_e32 v6, v6
	v_exp_f32_e32 v7, v7
	v_pk_fma_f32 v[8:9], v[8:9], v[84:85], v[48:49] op_sel_hi:[1,0,0] neg_lo:[0,0,1] neg_hi:[0,0,1]
	v_exp_f32_e32 v8, v8
	v_exp_f32_e32 v9, v9
	v_pk_fma_f32 v[10:11], v[10:11], v[84:85], v[48:49] op_sel_hi:[1,0,0] neg_lo:[0,0,1] neg_hi:[0,0,1]
	v_exp_f32_e32 v10, v10
	v_cvt_pk_f16_f32 v56, v2, v3
	v_cvt_pk_f16_f32 v57, v4, v5
	v_cvt_pk_f16_f32 v58, v6, v7
	v_cvt_pk_f16_f32 v59, v8, v9
	v_exp_f32_e32 v11, v11
	v_pk_fma_f32 v[12:13], v[12:13], v[84:85], v[48:49] op_sel_hi:[1,0,0] neg_lo:[0,0,1] neg_hi:[0,0,1]
	v_exp_f32_e32 v12, v12
	v_mfma_f32_32x32x16_f16 v[18:33], v[56:59], v[40:43], 0
	v_exp_f32_e32 v13, v13
	v_pk_fma_f32 v[14:15], v[14:15], v[84:85], v[48:49] op_sel_hi:[1,0,0] neg_lo:[0,0,1] neg_hi:[0,0,1]
	v_exp_f32_e32 v14, v14
	v_exp_f32_e32 v15, v15
	v_pk_fma_f32 v[16:17], v[16:17], v[84:85], v[48:49] op_sel_hi:[1,0,0] neg_lo:[0,0,1] neg_hi:[0,0,1]
	v_exp_f32_e32 v16, v16
	v_exp_f32_e32 v17, v17
	v_cvt_pk_f16_f32 v60, v10, v11
	v_cvt_pk_f16_f32 v61, v12, v13
	v_cvt_pk_f16_f32 v62, v14, v15
	v_cvt_pk_f16_f32 v63, v16, v17
	s_nop 1
	v_mfma_f32_32x32x16_f16 v[18:33], v[60:63], v[44:47], v[18:33]
	s_nop 11
	v_log_f32_e32 v18, v18
	v_log_f32_e32 v19, v19
	v_log_f32_e32 v20, v20
	v_log_f32_e32 v21, v21
	v_log_f32_e32 v22, v22
	v_log_f32_e32 v23, v23
	v_pk_fma_f32 v[64:65], v[18:19], v[84:85], v[64:65] op_sel:[0,1,0] op_sel_hi:[1,1,1]
	buffer_store_dword v64, v36, s[8:11], 0 offen
	buffer_store_dword v65, v36, s[8:11], s24 offen
	v_log_f32_e32 v24, v24
	v_log_f32_e32 v25, v25
	v_pk_fma_f32 v[66:67], v[20:21], v[84:85], v[66:67] op_sel:[0,1,0] op_sel_hi:[1,1,1]
	buffer_store_dword v66, v36, s[8:11], s25 offen
	buffer_store_dword v67, v36, s[8:11], s26 offen
	v_log_f32_e32 v26, v26
	v_log_f32_e32 v27, v27
	v_pk_fma_f32 v[68:69], v[22:23], v[84:85], v[68:69] op_sel:[0,1,0] op_sel_hi:[1,1,1]
	buffer_store_dword v68, v36, s[8:11], s27 offen
	buffer_store_dword v69, v36, s[8:11], s28 offen
	v_log_f32_e32 v28, v28
	v_log_f32_e32 v29, v29
	v_pk_fma_f32 v[70:71], v[24:25], v[84:85], v[70:71] op_sel:[0,1,0] op_sel_hi:[1,1,1]
	buffer_store_dword v70, v36, s[8:11], s29 offen
	buffer_store_dword v71, v36, s[8:11], s30 offen
	v_log_f32_e32 v30, v30
	v_log_f32_e32 v31, v31
	v_pk_fma_f32 v[72:73], v[26:27], v[84:85], v[72:73] op_sel:[0,1,0] op_sel_hi:[1,1,1]
	buffer_store_dword v72, v36, s[8:11], s31 offen
	buffer_store_dword v73, v36, s[8:11], s32 offen
	v_log_f32_e32 v32, v32
	v_log_f32_e32 v33, v33
	v_pk_fma_f32 v[74:75], v[28:29], v[84:85], v[74:75] op_sel:[0,1,0] op_sel_hi:[1,1,1]
	buffer_store_dword v74, v36, s[8:11], s33 offen
	buffer_store_dword v75, v36, s[8:11], s34 offen
	v_pk_fma_f32 v[76:77], v[30:31], v[84:85], v[76:77] op_sel:[0,1,0] op_sel_hi:[1,1,1]
	buffer_store_dword v76, v36, s[8:11], s35 offen
	buffer_store_dword v77, v36, s[8:11], s36 offen
	v_pk_fma_f32 v[78:79], v[32:33], v[84:85], v[78:79] op_sel:[0,1,0] op_sel_hi:[1,1,1]
	buffer_store_dword v78, v36, s[8:11], s37 offen
	buffer_store_dword v79, v36, s[8:11], s38 offen
	s_endpgm
